# LRU pass 1: the three per-unit gate-bias loads issued before the conv math (counted waits), no longer waited right after issue
# speedup vs baseline: 1.0074x; 1.0036x over previous
; #define LAS __attribute__((address_space(3)))
; DI unsigned pk_bf16(float lo, float hi) { f32x2 v = {lo, hi}; hbf16x2 r = __builtin_convertvector(v, hbf16x2); return __builtin_bit_cast(unsigned, r); }
; DI float bflo(unsigned w) { return __uint_as_float(w << 16); }
; DI float bfhi(unsigned w) { return __uint_as_float(w & 0xffff0000u); }
; template <int PASS>
; DI void lru_units(const Params& p, LAS unsigned char* lds, int G, int bid) {
;     ...
;         u32x2 grw[4];
;         {
;             const int c4 = (tid & 31) * 4, tb = 4 * (tid >> 5), cg = 128 * n + c4;
;             f32x4 xv[7];
; #pragma unroll
;             for (int q = 0; q < 7; ++q) { const int tt = t0 + tb + q - 2; u32x2 w = (u32x2){0u, 0u};
;                 if (tt >= 0 && tt < seg_len) w = *(const u32x2*)(Z + (size_t)(row0 + tb + q - 2) * L0INP + 832 + cg);
;                 xv[q] = (f32x4){bflo(w.x), bfhi(w.x), bflo(w.y), bfhi(w.y)}; }
;             if (PASS == 2) {
; #pragma unroll
;                 for (int j = 0; j < 4; ++j) grw[j] = *(const u32x2*)(Z + (size_t)(row0 + tb + j) * L0INP + 1856 + cg);
;             }
;             const f32x4 cb = *(const f32x4*)(p.in[17] + cg);
;             f32x4 cw[4];
; #pragma unroll
;             for (int tap = 0; tap < 4; ++tap) cw[tap] = *(const f32x4*)(p.in[16] + tap * 1024 + cg);
; #pragma unroll
;             for (int j = 0; j < 4; ++j) {
;                 const f32x4 acc = cb + xv[j] * cw[0] + xv[j + 1] * cw[1] + xv[j + 2] * cw[2] + xv[j + 3] * cw[3];
;                 *(LAS f32x4*)(U32 + (tb + j) * 128 + c4) = acc;
;                 u32x2 o; o.x = pk_bf16(acc[0], acc[1]); o.y = pk_bf16(acc[2], acc[3]);
;                 *(LAS u32x2*)(UBF + (tb + j) * 272 + c4 * 2) = o;
;             }
;         }
;         __syncthreads();
;     ...
;             const float ga_b = p.in[19][d * 1024 + chg], gx_b = p.in[21][d * 1024 + chg], lam = p.in[22][d * 1024 + chg];
.LBB0_357:
	s_or_b64 exec, exec, s[0:1]
	v_readlane_b32 s68, v251, 32
	v_lshlrev_b32_e32 v130, 2, v16
	v_readlane_b32 s69, v251, 33
	v_readlane_b32 s70, v251, 34
	v_readlane_b32 s71, v251, 35
	v_lshl_add_u64 v[32:33], s[68:69], 0, v[130:131]
	v_add_co_u32_e32 v28, vcc, s34, v32
	s_nop 2
	global_load_dwordx4 v[16:19], v130, s[70:71]
	global_load_dwordx4 v[20:23], v130, s[68:69]
	v_addc_co_u32_e32 v29, vcc, 0, v33, vcc
	v_add_co_u32_e32 v32, vcc, s35, v32
	global_load_dwordx4 v[24:27], v[28:29], off offset:-4096
	s_nop 0
	global_load_dwordx4 v[28:31], v[28:29], off
	v_addc_co_u32_e32 v33, vcc, 0, v33, vcc
	global_load_dwordx4 v[32:35], v[32:33], off
	s_waitcnt vmcnt(5)
	v_lshlrev_b32_e32 v46, 16, v2
	v_and_b32_e32 v47, 0xffff0000, v2
	v_lshlrev_b32_e32 v2, 16, v3
	v_and_b32_e32 v3, 0xffff0000, v3
	v_lshlrev_b32_e32 v40, 16, v8
	v_and_b32_e32 v41, 0xffff0000, v8
	v_lshlrev_b32_e32 v8, 16, v9
	v_and_b32_e32 v9, 0xffff0000, v9
	v_lshlrev_b32_e32 v42, 16, v6
	v_and_b32_e32 v43, 0xffff0000, v6
	v_lshlrev_b32_e32 v6, 16, v7
	v_and_b32_e32 v7, 0xffff0000, v7
	v_lshlrev_b32_e32 v44, 16, v4
	v_and_b32_e32 v45, 0xffff0000, v4
	v_lshlrev_b32_e32 v4, 16, v5
	v_and_b32_e32 v5, 0xffff0000, v5
	v_lshlrev_b32_e32 v48, 16, v14
	v_and_b32_e32 v49, 0xffff0000, v14
	v_lshlrev_b32_e32 v50, 16, v15
	v_and_b32_e32 v51, 0xffff0000, v15
	v_lshlrev_b32_e32 v38, 16, v10
	v_and_b32_e32 v39, 0xffff0000, v10
	v_lshlrev_b32_e32 v10, 16, v11
	v_and_b32_e32 v11, 0xffff0000, v11
	v_lshlrev_b32_e32 v36, 16, v12
	v_and_b32_e32 v37, 0xffff0000, v12
	v_lshlrev_b32_e32 v12, 16, v13
	v_and_b32_e32 v13, 0xffff0000, v13
	v_add_u32_e32 v58, v145, v147
	v_or_b32_e32 v159, s92, v1
	v_or_b32_e32 v130, v159, v140
	v_readlane_b32 s80, v251, 44
	v_readlane_b32 s81, v251, 45
	v_lshlrev_b32_e32 v130, 2, v130
	v_readlane_b32 s74, v251, 38
	v_readlane_b32 s75, v251, 39
	v_readlane_b32 s78, v251, 42
	v_readlane_b32 s79, v251, 43
	s_mul_i32 s0, s13, 36
	s_add_i32 s0, s0, s12
	s_ashr_i32 s1, s0, 31
	s_lshl_b64 s[0:1], s[0:1], 19
	v_readlane_b32 s72, v251, 36
	v_readlane_b32 s73, v251, 37
	v_readlane_b32 s76, v251, 40
	v_readlane_b32 s77, v251, 41
	v_readlane_b32 s82, v251, 46
	v_readlane_b32 s83, v251, 47
	global_load_dword v240, v130, s[80:81]
	global_load_dword v241, v130, s[74:75]
	global_load_dword v242, v130, s[78:79]
	s_waitcnt vmcnt(6)
	v_pk_fma_f32 v[2:3], v[22:23], v[2:3], v[18:19]
	v_pk_fma_f32 v[14:15], v[20:21], v[46:47], v[16:17]
	v_pk_fma_f32 v[46:47], v[22:23], v[4:5], v[18:19]
	v_pk_fma_f32 v[52:53], v[20:21], v[44:45], v[16:17]
	v_pk_fma_f32 v[54:55], v[22:23], v[6:7], v[18:19]
	v_pk_fma_f32 v[56:57], v[20:21], v[42:43], v[16:17]
	v_pk_fma_f32 v[18:19], v[22:23], v[8:9], v[18:19]
	v_pk_fma_f32 v[16:17], v[20:21], v[40:41], v[16:17]
	s_waitcnt vmcnt(5)
	v_pk_fma_f32 v[14:15], v[24:25], v[44:45], v[14:15]
	v_pk_fma_f32 v[2:3], v[26:27], v[4:5], v[2:3]
	v_pk_fma_f32 v[4:5], v[24:25], v[42:43], v[52:53]
	v_pk_fma_f32 v[20:21], v[26:27], v[6:7], v[46:47]
	v_pk_fma_f32 v[22:23], v[24:25], v[40:41], v[56:57]
	v_pk_fma_f32 v[44:45], v[26:27], v[8:9], v[54:55]
	v_pk_fma_f32 v[16:17], v[24:25], v[38:39], v[16:17]
	v_pk_fma_f32 v[18:19], v[26:27], v[10:11], v[18:19]
	s_waitcnt vmcnt(4)
	v_pk_fma_f32 v[6:7], v[30:31], v[6:7], v[2:3]
	v_pk_fma_f32 v[2:3], v[28:29], v[42:43], v[14:15]
	v_pk_fma_f32 v[14:15], v[30:31], v[8:9], v[20:21]
	v_pk_fma_f32 v[20:21], v[28:29], v[40:41], v[4:5]
	v_pk_fma_f32 v[24:25], v[30:31], v[10:11], v[44:45]
	v_pk_fma_f32 v[22:23], v[28:29], v[38:39], v[22:23]
	v_pk_fma_f32 v[18:19], v[30:31], v[12:13], v[18:19]
	v_pk_fma_f32 v[16:17], v[28:29], v[36:37], v[16:17]
	s_waitcnt vmcnt(3)
	v_pk_fma_f32 v[2:3], v[32:33], v[40:41], v[2:3]
	v_pk_fma_f32 v[4:5], v[34:35], v[8:9], v[6:7]
	v_pk_fma_f32 v[6:7], v[32:33], v[38:39], v[20:21]
	v_pk_fma_f32 v[8:9], v[34:35], v[10:11], v[14:15]
	v_pk_fma_f32 v[10:11], v[32:33], v[36:37], v[22:23]
	v_pk_fma_f32 v[12:13], v[34:35], v[12:13], v[24:25]
	v_pk_fma_f32 v[14:15], v[32:33], v[48:49], v[16:17]
	v_pk_fma_f32 v[16:17], v[34:35], v[50:51], v[18:19]
	ds_write_b128 v58, v[2:5]
	v_cvt_pk_bf16_f32 v2, v2, v3
	v_cvt_pk_bf16_f32 v3, v4, v5
	v_cvt_pk_bf16_f32 v4, v6, v7
	v_cvt_pk_bf16_f32 v5, v8, v9
	v_cvt_pk_bf16_f32 v18, v10, v11
	v_cvt_pk_bf16_f32 v19, v12, v13
	ds_write_b64 v149, v[2:3] offset:32768
	ds_write_b128 v150, v[6:9]
	ds_write_b64 v149, v[4:5] offset:33040
	ds_write_b128 v151, v[10:13]
	ds_write_b64 v149, v[18:19] offset:33312
	ds_write_b128 v152, v[14:17]
	v_cvt_pk_bf16_f32 v2, v14, v15
	v_cvt_pk_bf16_f32 v3, v16, v17
	ds_write_b64 v153, v[2:3] offset:32768
	s_waitcnt lgkmcnt(0)
	s_barrier
; #define LAS __attribute__((address_space(3)))
; template <int PASS>
; DI void lru_units(const Params& p, LAS unsigned char* lds, int G, int bid) {
;     ...
;         for (int ks = 0; ks < 8; ++ks) {
;             const bf16x8 a0 = *(const LAS bf16x8*)(UBF + jl * 272 + (16 * ks + 8 * h) * 2);
;             const bf16x8 a1 = *(const LAS bf16x8*)(UBF + (32 + jl) * 272 + (16 * ks + 8 * h) * 2);
;             acc[0][0] = __builtin_amdgcn_mfma_f32_32x32x16_bf16(a0, wa[ks], acc[0][0], 0, 0, 0);
;             acc[0][1] = __builtin_amdgcn_mfma_f32_32x32x16_bf16(a1, wa[ks], acc[0][1], 0, 0, 0);
;             acc[1][0] = __builtin_amdgcn_mfma_f32_32x32x16_bf16(a0, wx[ks], acc[1][0], 0, 0, 0);
;             acc[1][1] = __builtin_amdgcn_mfma_f32_32x32x16_bf16(a1, wx[ks], acc[1][1], 0, 0, 0);
;         }
;         {
;             const float ga_b = p.in[19][d * 1024 + chg], gx_b = p.in[21][d * 1024 + chg], lam = p.in[22][d * 1024 + chg];
;             const float sp8l2 = 8.0f * LOG2E * log1pf(expf(-lam));
	ds_read_b128 v[2:5], v154 offset:32768
	ds_read_b128 v[160:163], v154 offset:32800
	s_waitcnt lgkmcnt(1)
	v_mfma_f32_32x32x16_bf16 v[50:65], v[2:5], v[70:73], 0
	ds_read_b128 v[6:9], v154 offset:41472
	ds_read_b128 v[164:167], v154 offset:41504
	v_mfma_f32_32x32x16_bf16 v[34:49], v[2:5], v[66:69], 0
	s_waitcnt lgkmcnt(1)
	v_mfma_f32_32x32x16_bf16 v[18:33], v[6:9], v[70:73], 0
	v_mfma_f32_32x32x16_bf16 v[2:17], v[6:9], v[66:69], 0
	v_mfma_f32_32x32x16_bf16 v[50:65], v[160:163], v[78:81], v[50:65]
	v_mfma_f32_32x32x16_bf16 v[34:49], v[160:163], v[74:77], v[34:49]
	s_waitcnt lgkmcnt(0)
	v_mfma_f32_32x32x16_bf16 v[18:33], v[164:167], v[78:81], v[18:33]
	v_mfma_f32_32x32x16_bf16 v[2:17], v[164:167], v[74:77], v[2:17]
	ds_read_b128 v[160:163], v154 offset:32832
	ds_read_b128 v[164:167], v154 offset:32864
	ds_read_b128 v[168:171], v154 offset:41536
	ds_read_b128 v[172:175], v154 offset:41568
	s_waitcnt lgkmcnt(3)
	v_mfma_f32_32x32x16_bf16 v[50:65], v[160:163], v[86:89], v[50:65]
	v_mfma_f32_32x32x16_bf16 v[34:49], v[160:163], v[82:85], v[34:49]
	s_waitcnt lgkmcnt(1)
	v_mfma_f32_32x32x16_bf16 v[18:33], v[168:171], v[86:89], v[18:33]
	v_mfma_f32_32x32x16_bf16 v[2:17], v[168:171], v[82:85], v[2:17]
	v_mfma_f32_32x32x16_bf16 v[50:65], v[164:167], v[94:97], v[50:65]
	v_mfma_f32_32x32x16_bf16 v[34:49], v[164:167], v[90:93], v[34:49]
	ds_read_b128 v[160:163], v154 offset:32896
	ds_read_b128 v[164:167], v154 offset:32928
	s_waitcnt lgkmcnt(2)
	v_mfma_f32_32x32x16_bf16 v[18:33], v[172:175], v[94:97], v[18:33]
	v_mfma_f32_32x32x16_bf16 v[2:17], v[172:175], v[90:93], v[2:17]
	ds_read_b128 v[168:171], v154 offset:41600
	ds_read_b128 v[172:175], v154 offset:41632
	s_waitcnt lgkmcnt(3)
	v_mfma_f32_32x32x16_bf16 v[50:65], v[160:163], v[102:105], v[50:65]
	v_mfma_f32_32x32x16_bf16 v[34:49], v[160:163], v[98:101], v[34:49]
	s_waitcnt vmcnt(2)
	v_mov_b32_e32 v139, v240
	v_mul_f32_e32 v161, 0xbfb8aa3b, v139
	v_fma_f32 v162, v139, s40, -v161
	v_rndne_f32_e32 v163, v161
	v_fmac_f32_e32 v162, 0xb2a5705f, v139
	v_sub_f32_e32 v161, v161, v163
	v_add_f32_e32 v161, v161, v162
	v_cvt_i32_f32_e32 v163, v163
	v_exp_f32_e32 v161, v161
	v_cmp_nlt_f32_e32 vcc, s41, v139
	s_waitcnt lgkmcnt(2)
	v_mfma_f32_32x32x16_bf16 v[50:65], v[164:167], v[110:113], v[50:65]
	v_ldexp_f32 v161, v161, v163
	v_cndmask_b32_e32 v161, 0, v161, vcc
	v_cmp_ngt_f32_e32 vcc, s54, v139
	s_nop 1
	v_cndmask_b32_e32 v161, v158, v161, vcc
	v_add_f32_e32 v139, 1.0, v161
	v_add_f32_e32 v188, -1.0, v139
	v_frexp_mant_f32_e32 v189, v139
	v_cvt_f64_f32_e32 v[162:163], v139
	v_sub_f32_e32 v190, v188, v139
	v_frexp_exp_i32_f64_e32 v162, v[162:163]
	v_cmp_gt_f32_e32 vcc, s58, v189
	v_sub_f32_e32 v188, v161, v188
	v_add_f32_e32 v163, 1.0, v190
	v_subbrev_co_u32_e32 v189, vcc, 0, v162, vcc
	v_add_f32_e32 v162, v188, v163
	v_sub_u32_e32 v163, 0, v189
	v_ldexp_f32 v139, v139, v163
	v_mfma_f32_32x32x16_bf16 v[34:49], v[164:167], v[106:109], v[34:49]
	v_add_f32_e32 v164, -1.0, v139
	v_add_f32_e32 v165, 1.0, v139
	v_ldexp_f32 v162, v162, v163
	v_add_f32_e32 v163, 1.0, v164
	v_add_f32_e32 v166, -1.0, v165
	v_sub_f32_e32 v163, v139, v163
	v_sub_f32_e32 v139, v139, v166
	s_waitcnt lgkmcnt(1)
	v_mfma_f32_32x32x16_bf16 v[18:33], v[168:171], v[102:105], v[18:33]
	v_add_f32_e32 v139, v162, v139
	v_add_f32_e32 v188, v165, v139
	v_rcp_f32_e32 v190, v188
	v_add_f32_e32 v166, v162, v163
	v_add_f32_e32 v163, v164, v166
	v_sub_f32_e32 v164, v164, v163
	v_sub_f32_e32 v162, v165, v188
	v_mfma_f32_32x32x16_bf16 v[2:17], v[168:171], v[98:101], v[2:17]
	v_add_f32_e32 v139, v139, v162
	ds_read_b128 v[168:171], v154 offset:32960
	ds_read_b128 v[176:179], v154 offset:32992
	v_cmp_neq_f32_e32 vcc, s55, v161
	ds_read_b128 v[180:183], v154 offset:41664
	ds_read_b128 v[184:187], v154 offset:41696
	s_waitcnt lgkmcnt(4)
	v_mfma_f32_32x32x16_bf16 v[18:33], v[172:175], v[110:113], v[18:33]
	v_mfma_f32_32x32x16_bf16 v[2:17], v[172:175], v[106:109], v[2:17]
	v_mul_f32_e32 v173, v163, v190
	v_add_f32_e32 v172, v166, v164
	v_mul_f32_e32 v164, v188, v173
	v_fma_f32 v166, v173, v188, -v164
	v_fmac_f32_e32 v166, v173, v139
	v_add_f32_e32 v162, v164, v166
	v_sub_f32_e32 v165, v163, v162
	v_mov_b32_e32 v167, v162
	v_pk_add_f32 v[162:163], v[162:163], v[164:165] neg_lo:[0,1] neg_hi:[0,1]
	s_waitcnt lgkmcnt(3)
	v_mfma_f32_32x32x16_bf16 v[50:65], v[168:171], v[118:121], v[50:65]
	v_add_f32_e64 v162, v162, -v166
	v_add_f32_e64 v163, v163, -v167
	v_add_f32_e32 v163, v172, v163
	v_add_f32_e32 v162, v162, v163
	v_add_f32_e32 v163, v165, v162
	v_mul_f32_e32 v172, v190, v163
	v_mul_f32_e32 v164, v188, v172
	v_fma_f32 v166, v172, v188, -v164
	v_sub_f32_e32 v165, v165, v163
	v_fmac_f32_e32 v166, v172, v139
	v_add_f32_e32 v174, v162, v165
	v_add_f32_e32 v162, v164, v166
	v_sub_f32_e32 v165, v163, v162
	v_mov_b32_e32 v167, v162
	v_pk_add_f32 v[162:163], v[162:163], v[164:165] neg_lo:[0,1] neg_hi:[0,1]
	v_add_f32_e32 v175, v173, v172
	v_pk_add_f32 v[162:163], v[162:163], v[166:167] neg_lo:[0,1] neg_hi:[0,1]
	v_sub_f32_e32 v173, v175, v173
	v_add_f32_e32 v139, v174, v163
	v_add_f32_e32 v139, v162, v139
	v_add_f32_e32 v139, v165, v139
	v_mul_f32_e32 v139, v190, v139
	v_sub_f32_e32 v162, v172, v173
	v_add_f32_e32 v163, v162, v139
	v_add_f32_e32 v164, v175, v163
	v_cvt_f32_i32_e32 v162, v189
	v_mul_f32_e32 v166, v164, v164
	v_sub_f32_e32 v165, v164, v175
	v_fmamk_f32 v139, v166, 0x3e9b6dac, v155
	v_sub_f32_e32 v163, v163, v165
	v_mfma_f32_32x32x16_bf16 v[34:49], v[168:171], v[114:117], v[34:49]
	v_fmaak_f32 v139, v166, v139, 0x3f2aaada
	v_ldexp_f32 v168, v163, 1
	v_mul_f32_e32 v163, v164, v166
	v_mul_f32_e64 v166, v162, v138
	v_mul_f32_e64 v167, v163, v139
	v_ldexp_f32 v165, v164, 1
	v_fma_f32 v164, v162, s59, -v166
	v_fmac_f32_e32 v164, 0xb102e308, v162
	v_pk_add_f32 v[162:163], v[166:167], v[164:165]
	s_waitcnt lgkmcnt(2)
; #define LAS __attribute__((address_space(3)))
; template <int PASS>
; DI void lru_units(const Params& p, LAS unsigned char* lds, int G, int bid) {
;     ...
;         for (int ks = 0; ks < 8; ++ks) {
;             const bf16x8 a0 = *(const LAS bf16x8*)(UBF + jl * 272 + (16 * ks + 8 * h) * 2);
;             const bf16x8 a1 = *(const LAS bf16x8*)(UBF + (32 + jl) * 272 + (16 * ks + 8 * h) * 2);
;             acc[0][0] = __builtin_amdgcn_mfma_f32_32x32x16_bf16(a0, wa[ks], acc[0][0], 0, 0, 0);
;             acc[0][1] = __builtin_amdgcn_mfma_f32_32x32x16_bf16(a1, wa[ks], acc[0][1], 0, 0, 0);
;             acc[1][0] = __builtin_amdgcn_mfma_f32_32x32x16_bf16(a0, wx[ks], acc[1][0], 0, 0, 0);
;             acc[1][1] = __builtin_amdgcn_mfma_f32_32x32x16_bf16(a1, wx[ks], acc[1][1], 0, 0, 0);
;         }
;         {
;             const float ga_b = p.in[19][d * 1024 + chg], gx_b = p.in[21][d * 1024 + chg], lam = p.in[22][d * 1024 + chg];
;             const float sp8l2 = 8.0f * LOG2E * log1pf(expf(-lam));
; #pragma unroll
;             for (int mt = 0; mt < 2; ++mt)
; #pragma unroll
;                 for (int i = 0; i < 16; ++i) {
;                     const int t = 32 * mt + (i & 3) + 8 * (i >> 2) + 4 * h;
;                     const float r = __builtin_amdgcn_rcpf(1.0f + __builtin_amdgcn_exp2f(-LOG2E * (acc[0][mt][i] + ga_b)));
;                     const float ig = __builtin_amdgcn_rcpf(1.0f + __builtin_amdgcn_exp2f(-LOG2E * (acc[1][mt][i] + gx_b)));
;                     const float a = __builtin_amdgcn_exp2f(-sp8l2 * r);
;                     const float bb = __builtin_amdgcn_sqrtf((1.0f - a) * (1.0f + a)) * (ig * U32[t * 128 + ch]);
;                     acc[0][mt][i] = a; acc[1][mt][i] = bb;
;                 }
	v_mfma_f32_32x32x16_bf16 v[50:65], v[176:179], v[126:129], v[50:65]
	v_sub_f32_e32 v139, v163, v165
	v_sub_f32_e32 v139, v167, v139
	v_add_f32_e32 v169, v168, v139
	v_mov_b32_e32 v168, v166
	v_add_f32_e64 v166, v162, -v166
	v_add_f32_e64 v167, v163, -v167
	v_pk_add_f32 v[170:171], v[162:163], v[168:169]
	v_mov_b32_e32 v165, v162
	v_mov_b32_e32 v167, v171
	v_pk_add_f32 v[172:173], v[164:165], v[166:167] neg_lo:[0,1] neg_hi:[0,1]
	v_pk_add_f32 v[164:165], v[164:165], v[166:167]
	v_mov_b32_e32 v168, v169
	v_pk_add_f32 v[166:167], v[164:165], v[162:163] op_sel:[1,0] op_sel_hi:[0,1] neg_lo:[0,1] neg_hi:[0,1]
	v_pk_add_f32 v[174:175], v[170:171], v[166:167] op_sel_hi:[1,0] neg_lo:[0,1] neg_hi:[0,1]
	v_mov_b32_e32 v170, v171
	v_mov_b32_e32 v171, v165
	v_pk_mov_b32 v[166:167], v[162:163], v[166:167] op_sel:[1,0]
	v_mov_b32_e32 v169, v162
	v_pk_add_f32 v[166:167], v[170:171], v[166:167] neg_lo:[0,1] neg_hi:[0,1]
	v_mov_b32_e32 v174, v172
	v_pk_add_f32 v[162:163], v[168:169], v[166:167] neg_lo:[0,1] neg_hi:[0,1]
	v_mov_b32_e32 v173, v165
	v_pk_add_f32 v[166:167], v[174:175], v[162:163]
	v_mfma_f32_32x32x16_bf16 v[34:49], v[176:179], v[122:125], v[34:49]
	v_add_f32_e64 v168, v166, v167
	v_add_f32_e64 v169, v167, v166
	s_waitcnt vmcnt(1)
	v_mov_b32_e32 v160, v241
	v_add_f32_e32 v50, v50, v160
	v_pk_add_f32 v[164:165], v[164:165], v[168:169] op_sel:[1,0] op_sel_hi:[0,1]
	v_mov_b32_e32 v167, v164
	v_pk_add_f32 v[170:171], v[166:167], v[172:173] neg_lo:[0,1] neg_hi:[0,1]
	v_mov_b32_e32 v163, v168
	v_sub_f32_e32 v139, v166, v170
	v_pk_add_f32 v[162:163], v[162:163], v[170:171] neg_lo:[0,1] neg_hi:[0,1]
	v_sub_f32_e32 v139, v172, v139
	v_mul_f32_e32 v50, 0xbfb8aa3b, v50
	v_add_f32_e32 v139, v162, v139
	v_exp_f32_e32 v50, v50
	v_add_f32_e32 v139, v139, v163
	v_add_f32_e32 v139, v164, v139
	v_cndmask_b32_e32 v139, v158, v139, vcc
	v_cmp_lt_f32_e64 vcc, |v161|, s66
	s_waitcnt vmcnt(0)
	v_mov_b32_e32 v130, v242
	v_add_f32_e32 v34, v34, v130
	v_add_f32_e32 v50, 1.0, v50
	v_cndmask_b32_e32 v139, v139, v161, vcc
	v_mul_f32_e32 v34, 0xbfb8aa3b, v34
	v_mul_f32_e32 v164, 0xc138aa3b, v139
	v_rcp_f32_e32 v50, v50
	v_exp_f32_e32 v139, v34
	v_add_f32_e32 v51, v51, v160
	ds_read2st64_b32 v[166:167], v156 offset1:2
	v_mul_f32_e32 v34, v50, v164
	v_add_f32_e32 v50, 1.0, v139
	v_mul_f32_e32 v51, 0xbfb8aa3b, v51
	v_rcp_f32_e32 v139, v50
	v_exp_f32_e32 v161, v51
	v_add_f32_e32 v52, v52, v160
	v_mul_f32_e32 v52, 0xbfb8aa3b, v52
	s_waitcnt lgkmcnt(0)
	v_mul_f32_e32 v51, v166, v139
	v_add_f32_e32 v139, 1.0, v161
	v_rcp_f32_e32 v139, v139
	v_exp_f32_e32 v52, v52
	v_add_f32_e32 v35, v35, v130
	v_mul_f32_e32 v35, 0xbfb8aa3b, v35
	v_exp_f32_e32 v161, v35
	v_mul_f32_e32 v35, v139, v164
	v_exp_f32_e32 v35, v35
	v_add_f32_e32 v52, 1.0, v52
	v_add_f32_e32 v53, v53, v160
	v_rcp_f32_e32 v52, v52
	v_mul_f32_e32 v53, 0xbfb8aa3b, v53
	v_exp_f32_e32 v53, v53
	v_add_f32_e32 v36, v36, v130
	v_add_f32_e32 v161, 1.0, v161
	v_sub_f32_e32 v165, 1.0, v35
	v_add_f32_e32 v163, 1.0, v35
	v_mul_f32_e32 v36, 0xbfb8aa3b, v36
	v_rcp_f32_e32 v161, v161
	v_mul_f32_e32 v163, v165, v163
	v_exp_f32_e32 v166, v36
	v_mul_f32_e32 v36, v52, v164
	v_sqrt_f32_e32 v163, v163
	v_exp_f32_e32 v36, v36
	v_add_f32_e32 v53, 1.0, v53
	v_rcp_f32_e32 v53, v53
	v_add_f32_e32 v54, v54, v160
	v_mul_f32_e32 v54, 0xbfb8aa3b, v54
	v_mul_f32_e32 v161, v167, v161
	v_add_f32_e32 v37, v37, v130
	v_exp_f32_e32 v54, v54
	v_mul_f32_e32 v52, v161, v163
	v_add_f32_e32 v161, 1.0, v166
	v_sub_f32_e32 v166, 1.0, v36
	v_add_f32_e32 v163, 1.0, v36
	ds_read2st64_b32 v[168:169], v156 offset0:4 offset1:6
	v_mul_f32_e32 v37, 0xbfb8aa3b, v37
	v_rcp_f32_e32 v161, v161
	v_mul_f32_e32 v163, v166, v163
	v_exp_f32_e32 v167, v37
	v_mul_f32_e32 v37, v53, v164
	v_sqrt_f32_e32 v163, v163
	v_exp_f32_e32 v37, v37
	v_add_f32_e32 v54, 1.0, v54
	v_rcp_f32_e32 v54, v54
	s_waitcnt lgkmcnt(0)
	v_mul_f32_e32 v161, v168, v161
	v_mul_f32_e32 v53, v161, v163
	v_add_f32_e32 v161, 1.0, v167
	v_sub_f32_e32 v167, 1.0, v37
	v_add_f32_e32 v163, 1.0, v37
	v_add_f32_e32 v38, v38, v130
	v_rcp_f32_e32 v161, v161
	v_mul_f32_e32 v163, v167, v163
	v_mul_f32_e32 v38, 0xbfb8aa3b, v38
	v_sqrt_f32_e32 v163, v163
	v_exp_f32_e32 v168, v38
	v_mul_f32_e32 v38, v54, v164
	v_add_f32_e32 v55, v55, v160
	v_exp_f32_e32 v38, v38
	v_mul_f32_e32 v55, 0xbfb8aa3b, v55
	v_exp_f32_e32 v171, v55
	v_mul_f32_e32 v161, v169, v161
	v_mul_f32_e32 v54, v161, v163
	v_add_f32_e32 v161, 1.0, v168
	ds_read2st64_b32 v[168:169], v156 offset0:16 offset1:18
	v_rcp_f32_e32 v161, v161
	v_sub_f32_e32 v170, 1.0, v38
	v_add_f32_e32 v163, 1.0, v38
	v_mul_f32_e32 v55, v170, v163
	v_add_f32_e32 v163, 1.0, v171
	v_rcp_f32_e32 v163, v163
	v_add_f32_e32 v39, v39, v130
	v_mul_f32_e32 v39, 0xbfb8aa3b, v39
	s_waitcnt lgkmcnt(0)
	v_mul_f32_e32 v161, v161, v168
	v_exp_f32_e32 v168, v39
	v_add_f32_e32 v56, v56, v160
	v_mul_f32_e32 v39, v163, v164
	v_mul_f32_e32 v56, 0xbfb8aa3b, v56
	v_exp_f32_e32 v39, v39
	v_exp_f32_e32 v56, v56
	v_add_f32_e32 v168, 1.0, v168
	v_rcp_f32_e32 v168, v168
	v_sub_f32_e32 v171, 1.0, v39
	v_add_f32_e32 v172, 1.0, v39
	v_add_f32_e32 v56, 1.0, v56
	v_add_f32_e32 v40, v40, v130
	v_mul_f32_e32 v172, v171, v172
	v_rcp_f32_e32 v56, v56
	v_mul_f32_e32 v40, 0xbfb8aa3b, v40
	v_sqrt_f32_e32 v172, v172
	v_mul_f32_e32 v168, v168, v169
	v_exp_f32_e32 v169, v40
	v_add_f32_e32 v57, v57, v160
	v_mul_f32_e32 v57, 0xbfb8aa3b, v57
	v_mul_f32_e32 v40, v56, v164
	v_exp_f32_e32 v57, v57
	v_exp_f32_e32 v40, v40
	v_mul_f32_e32 v56, v168, v172
	v_add_f32_e32 v168, 1.0, v169
	v_rcp_f32_e32 v173, v168
	ds_read2st64_b32 v[168:169], v156 offset0:20 offset1:22
	v_add_f32_e32 v57, 1.0, v57
	v_sub_f32_e32 v172, 1.0, v40
	v_add_f32_e32 v174, 1.0, v40
	v_rcp_f32_e32 v57, v57
	v_add_f32_e32 v41, v41, v130
	v_add_f32_e32 v58, v58, v160
	v_mul_f32_e32 v174, v172, v174
	v_mul_f32_e32 v41, 0xbfb8aa3b, v41
	v_mul_f32_e32 v58, 0xbfb8aa3b, v58
	v_sqrt_f32_e32 v174, v174
	s_waitcnt lgkmcnt(0)
; template <int PASS>
; DI void lru_units(const Params& p, LAS unsigned char* lds, int G, int bid) {
;     ...
;                 for (int i = 0; i < 16; ++i) {
;                     const int t = 32 * mt + (i & 3) + 8 * (i >> 2) + 4 * h;
;                     const float r = __builtin_amdgcn_rcpf(1.0f + __builtin_amdgcn_exp2f(-LOG2E * (acc[0][mt][i] + ga_b)));
;                     const float ig = __builtin_amdgcn_rcpf(1.0f + __builtin_amdgcn_exp2f(-LOG2E * (acc[1][mt][i] + gx_b)));
;                     const float a = __builtin_amdgcn_exp2f(-sp8l2 * r);
;                     const float bb = __builtin_amdgcn_sqrtf((1.0f - a) * (1.0f + a)) * (ig * U32[t * 128 + ch]);
;                     acc[0][mt][i] = a; acc[1][mt][i] = bb;
;                 }
	v_mul_f32_e32 v168, v173, v168
	v_exp_f32_e32 v173, v41
	v_exp_f32_e32 v58, v58
	v_mul_f32_e32 v41, v57, v164
	v_exp_f32_e32 v41, v41
	v_mul_f32_e32 v57, v168, v174
	v_add_f32_e32 v168, 1.0, v173
	v_add_f32_e32 v58, 1.0, v58
	v_rcp_f32_e32 v168, v168
	v_rcp_f32_e32 v58, v58
	v_sub_f32_e32 v173, 1.0, v41
	v_add_f32_e32 v174, 1.0, v41
	v_add_f32_e32 v42, v42, v130
	v_mul_f32_e32 v174, v173, v174
	v_mul_f32_e32 v42, 0xbfb8aa3b, v42
	v_sqrt_f32_e32 v174, v174
	v_mul_f32_e32 v168, v168, v169
	v_exp_f32_e32 v169, v42
	v_mul_f32_e32 v42, v58, v164
	v_add_f32_e32 v59, v59, v160
	v_exp_f32_e32 v42, v42
	v_mul_f32_e32 v59, 0xbfb8aa3b, v59
	v_exp_f32_e32 v177, v59
	v_mul_f32_e32 v58, v168, v174
	v_add_f32_e32 v168, 1.0, v169
	ds_read2st64_b32 v[174:175], v156 offset0:32 offset1:34
	v_rcp_f32_e32 v168, v168
	v_sub_f32_e32 v176, 1.0, v42
	v_add_f32_e32 v169, 1.0, v42
	v_mul_f32_e32 v59, v176, v169
	v_add_f32_e32 v169, 1.0, v177
	v_rcp_f32_e32 v169, v169
	v_add_f32_e32 v43, v43, v130
	v_mul_f32_e32 v43, 0xbfb8aa3b, v43
	s_waitcnt lgkmcnt(0)
	v_mul_f32_e32 v168, v168, v174
	v_exp_f32_e32 v174, v43
	v_add_f32_e32 v60, v60, v160
	v_mul_f32_e32 v43, v169, v164
	v_mul_f32_e32 v60, 0xbfb8aa3b, v60
	v_exp_f32_e32 v43, v43
	v_exp_f32_e32 v60, v60
	v_add_f32_e32 v174, 1.0, v174
	v_rcp_f32_e32 v174, v174
	v_sub_f32_e32 v177, 1.0, v43
	v_add_f32_e32 v178, 1.0, v43
	v_add_f32_e32 v60, 1.0, v60
	v_add_f32_e32 v44, v44, v130
	v_mul_f32_e32 v178, v177, v178
	v_rcp_f32_e32 v60, v60
	v_mul_f32_e32 v44, 0xbfb8aa3b, v44
	v_add_f32_e32 v61, v61, v160
	v_sqrt_f32_e32 v178, v178
	v_mul_f32_e32 v174, v174, v175
	v_exp_f32_e32 v175, v44
	v_mul_f32_e32 v61, 0xbfb8aa3b, v61
	v_exp_f32_e32 v61, v61
	v_mul_f32_e32 v44, v60, v164
	v_exp_f32_e32 v44, v44
	v_mul_f32_e32 v60, v174, v178
	v_add_f32_e32 v174, 1.0, v175
	v_rcp_f32_e32 v179, v174
	ds_read2st64_b32 v[174:175], v156 offset0:36 offset1:38
	v_add_f32_e32 v61, 1.0, v61
	v_rcp_f32_e32 v61, v61
	v_mfma_f32_32x32x16_bf16 v[18:33], v[180:183], v[118:121], v[18:33]
	v_sub_f32_e32 v178, 1.0, v44
	v_add_f32_e32 v45, v45, v130
	v_add_f32_e32 v62, v62, v160
	v_mul_f32_e32 v45, 0xbfb8aa3b, v45
	v_mul_f32_e32 v62, 0xbfb8aa3b, v62
	s_waitcnt lgkmcnt(0)
	v_mul_f32_e32 v174, v179, v174
	v_exp_f32_e32 v179, v45
	v_mfma_f32_32x32x16_bf16 v[2:17], v[180:183], v[114:117], v[2:17]
	v_add_f32_e32 v180, 1.0, v44
	v_mul_f32_e32 v180, v178, v180
	v_sqrt_f32_e32 v180, v180
	v_mul_f32_e32 v45, v61, v164
	v_exp_f32_e32 v62, v62
	v_exp_f32_e32 v45, v45
	v_mul_f32_e32 v61, v174, v180
	v_add_f32_e32 v174, 1.0, v179
	v_add_f32_e32 v62, 1.0, v62
	v_rcp_f32_e32 v174, v174
	v_sub_f32_e32 v180, 1.0, v45
	v_add_f32_e32 v179, 1.0, v45
	v_rcp_f32_e32 v62, v62
	v_mul_f32_e32 v179, v180, v179
	v_sqrt_f32_e32 v179, v179
	v_add_f32_e32 v46, v46, v130
	v_mul_f32_e32 v46, 0xbfb8aa3b, v46
	v_mul_f32_e32 v174, v174, v175
	v_exp_f32_e32 v175, v46
	v_mul_f32_e32 v46, v62, v164
	v_add_f32_e32 v63, v63, v160
	v_exp_f32_e32 v46, v46
	v_mul_f32_e32 v63, 0xbfb8aa3b, v63
	v_mul_f32_e32 v62, v174, v179
	v_exp_f32_e32 v179, v63
	v_add_f32_e32 v174, 1.0, v175
	v_sub_f32_e32 v182, 1.0, v46
	v_add_f32_e32 v175, 1.0, v46
	v_mul_f32_e32 v63, v182, v175
	v_add_f32_e32 v175, 1.0, v179
	v_rcp_f32_e32 v175, v175
	v_add_f32_e32 v47, v47, v130
	v_mul_f32_e32 v47, 0xbfb8aa3b, v47
	v_add_f32_e32 v64, v64, v160
	v_exp_f32_e32 v179, v47
	v_mul_f32_e32 v47, v175, v164
	v_mul_f32_e32 v64, 0xbfb8aa3b, v64
	v_exp_f32_e32 v47, v47
	v_exp_f32_e32 v64, v64
	v_mfma_f32_32x32x16_bf16 v[18:33], v[184:187], v[126:129], v[18:33]
	v_rcp_f32_e32 v174, v174
	v_add_f32_e32 v179, 1.0, v179
	v_sub_f32_e32 v183, 1.0, v47
	v_add_f32_e32 v181, 1.0, v47
	v_add_f32_e32 v64, 1.0, v64
	v_add_f32_e32 v48, v48, v130
	v_add_f32_e32 v65, v65, v160
	v_mfma_f32_32x32x16_bf16 v[2:17], v[184:187], v[122:125], v[2:17]
	ds_read2st64_b32 v[184:185], v156 offset0:48 offset1:50
	v_rcp_f32_e32 v179, v179
	v_mul_f32_e32 v181, v183, v181
	v_rcp_f32_e32 v64, v64
	v_mul_f32_e32 v48, 0xbfb8aa3b, v48
	v_mul_f32_e32 v65, 0xbfb8aa3b, v65
	s_waitcnt lgkmcnt(0)
	v_mul_f32_e32 v174, v174, v184
	v_sqrt_f32_e32 v181, v181
	v_exp_f32_e32 v184, v48
	v_exp_f32_e32 v65, v65
	v_mul_f32_e32 v179, v179, v185
	v_mul_f32_e32 v48, v64, v164
	v_exp_f32_e32 v48, v48
	v_mul_f32_e32 v64, v179, v181
	v_add_f32_e32 v179, 1.0, v184
	ds_read2st64_b32 v[184:185], v156 offset0:52 offset1:54
	v_add_f32_e32 v65, 1.0, v65
	v_rcp_f32_e32 v179, v179
	v_rcp_f32_e32 v65, v65
	v_add_f32_e32 v18, v18, v160
	v_mul_f32_e32 v18, 0xbfb8aa3b, v18
	v_add_f32_e32 v49, v49, v130
	v_exp_f32_e32 v18, v18
	v_sub_f32_e32 v186, 1.0, v48
	v_add_f32_e32 v181, 1.0, v48
	v_mul_f32_e32 v49, 0xbfb8aa3b, v49
	v_mul_f32_e32 v181, v186, v181
	s_waitcnt lgkmcnt(0)
	v_mul_f32_e32 v179, v179, v184
	v_exp_f32_e32 v184, v49
	v_mul_f32_e32 v49, v65, v164
	v_sqrt_f32_e32 v181, v181
	v_exp_f32_e32 v49, v49
	v_add_f32_e32 v18, 1.0, v18
	v_rcp_f32_e32 v18, v18
	v_mul_f32_e32 v65, v179, v181
	v_add_f32_e32 v179, 1.0, v184
	v_sub_f32_e32 v187, 1.0, v49
	v_add_f32_e32 v181, 1.0, v49
	v_add_f32_e32 v2, v2, v130
	v_rcp_f32_e32 v179, v179
	v_mul_f32_e32 v181, v187, v181
	v_mul_f32_e32 v2, 0xbfb8aa3b, v2
	v_sqrt_f32_e32 v181, v181
	v_exp_f32_e32 v184, v2
	v_mul_f32_e32 v2, v18, v164
	v_add_f32_e32 v19, v19, v160
	v_exp_f32_e32 v2, v2
	v_mul_f32_e32 v19, 0xbfb8aa3b, v19
	v_exp_f32_e32 v189, v19
	v_mul_f32_e32 v179, v179, v185
	v_mul_f32_e32 v18, v179, v181
	v_add_f32_e32 v179, 1.0, v184
	ds_read2st64_b32 v[184:185], v156 offset0:64 offset1:66
	v_rcp_f32_e32 v179, v179
	v_sub_f32_e32 v188, 1.0, v2
	v_add_f32_e32 v181, 1.0, v2
	v_mul_f32_e32 v19, v188, v181
	v_add_f32_e32 v181, 1.0, v189
	v_rcp_f32_e32 v181, v181
	v_add_f32_e32 v3, v3, v130
	v_add_f32_e32 v20, v20, v160
	v_mul_f32_e32 v3, 0xbfb8aa3b, v3
	v_mul_f32_e32 v20, 0xbfb8aa3b, v20
	s_waitcnt lgkmcnt(0)
; template <int PASS>
; DI void lru_units(const Params& p, LAS unsigned char* lds, int G, int bid) {
;     ...
;                 for (int i = 0; i < 16; ++i) {
;                     const int t = 32 * mt + (i & 3) + 8 * (i >> 2) + 4 * h;
;                     const float r = __builtin_amdgcn_rcpf(1.0f + __builtin_amdgcn_exp2f(-LOG2E * (acc[0][mt][i] + ga_b)));
;                     const float ig = __builtin_amdgcn_rcpf(1.0f + __builtin_amdgcn_exp2f(-LOG2E * (acc[1][mt][i] + gx_b)));
;                     const float a = __builtin_amdgcn_exp2f(-sp8l2 * r);
;                     const float bb = __builtin_amdgcn_sqrtf((1.0f - a) * (1.0f + a)) * (ig * U32[t * 128 + ch]);
;                     acc[0][mt][i] = a; acc[1][mt][i] = bb;
;                 }
	v_mul_f32_e32 v179, v179, v184
	v_exp_f32_e32 v184, v3
	v_exp_f32_e32 v20, v20
	v_mul_f32_e32 v3, v181, v164
	v_exp_f32_e32 v3, v3
	v_add_f32_e32 v184, 1.0, v184
	v_add_f32_e32 v20, 1.0, v20
	v_add_f32_e32 v21, v21, v160
	v_rcp_f32_e32 v184, v184
	v_rcp_f32_e32 v20, v20
	v_mul_f32_e32 v21, 0xbfb8aa3b, v21
	v_exp_f32_e32 v21, v21
	v_sub_f32_e32 v189, 1.0, v3
	v_add_f32_e32 v190, 1.0, v3
	v_add_f32_e32 v4, v4, v130
	v_mul_f32_e32 v190, v189, v190
	v_mul_f32_e32 v4, 0xbfb8aa3b, v4
	v_sqrt_f32_e32 v190, v190
	v_mul_f32_e32 v184, v184, v185
	v_exp_f32_e32 v185, v4
	v_mul_f32_e32 v4, v20, v164
	v_exp_f32_e32 v4, v4
	v_add_f32_e32 v21, 1.0, v21
	v_rcp_f32_e32 v21, v21
	v_mul_f32_e32 v20, v184, v190
	v_add_f32_e32 v184, 1.0, v185
	v_rcp_f32_e32 v190, v184
	v_sub_f32_e32 v191, 1.0, v4
	v_add_f32_e32 v192, 1.0, v4
	ds_read2st64_b32 v[184:185], v156 offset0:68 offset1:70
	v_add_f32_e32 v5, v5, v130
	v_mul_f32_e32 v192, v191, v192
	v_mul_f32_e32 v5, 0xbfb8aa3b, v5
	v_mul_f32_e32 v21, v21, v164
	v_sqrt_f32_e32 v192, v192
	v_exp_f32_e32 v5, v5
	v_exp_f32_e32 v21, v21
	v_add_f32_e32 v22, v22, v160
	v_mul_f32_e32 v22, 0xbfb8aa3b, v22
	v_exp_f32_e32 v22, v22
	s_waitcnt lgkmcnt(0)
	v_mul_f32_e32 v184, v190, v184
	v_mul_f32_e32 v190, v184, v192
	v_add_f32_e32 v5, 1.0, v5
	v_sub_f32_e32 v192, 1.0, v21
	v_add_f32_e32 v184, 1.0, v21
	v_add_f32_e32 v6, v6, v130
	v_rcp_f32_e32 v5, v5
	v_mul_f32_e32 v184, v192, v184
	v_mul_f32_e32 v6, 0xbfb8aa3b, v6
	v_sqrt_f32_e32 v184, v184
	v_add_f32_e32 v22, 1.0, v22
	v_exp_f32_e32 v6, v6
	v_rcp_f32_e32 v22, v22
	v_mul_f32_e32 v5, v5, v185
	v_add_f32_e32 v23, v23, v160
	v_mul_f32_e32 v193, v5, v184
	v_add_f32_e32 v5, 1.0, v6
	ds_read2st64_b32 v[184:185], v156 offset0:80 offset1:82
	v_mul_f32_e32 v23, 0xbfb8aa3b, v23
	v_mul_f32_e32 v22, v22, v164
	v_rcp_f32_e32 v5, v5
	v_exp_f32_e32 v23, v23
	v_exp_f32_e32 v22, v22
	v_add_f32_e32 v8, v8, v130
	s_waitcnt lgkmcnt(0)
	v_mul_f32_e32 v184, v5, v184
	v_add_f32_e32 v5, 1.0, v23
	v_sub_f32_e32 v194, 1.0, v22
	v_add_f32_e32 v6, 1.0, v22
	v_rcp_f32_e32 v5, v5
	v_mul_f32_e32 v6, v194, v6
	v_sqrt_f32_e32 v195, v6
	v_add_f32_e32 v6, v7, v130
	v_add_f32_e32 v7, v24, v160
	v_mul_f32_e32 v7, 0xbfb8aa3b, v7
	v_mul_f32_e32 v6, 0xbfb8aa3b, v6
	v_mul_f32_e32 v5, v5, v164
	v_exp_f32_e32 v7, v7
	v_exp_f32_e32 v6, v6
	v_exp_f32_e32 v23, v5
	v_mul_f32_e32 v8, 0xbfb8aa3b, v8
	v_add_f32_e32 v7, 1.0, v7
	v_add_f32_e32 v5, 1.0, v6
	v_sub_f32_e32 v197, 1.0, v23
	v_add_f32_e32 v6, 1.0, v23
	v_rcp_f32_e32 v7, v7
	v_rcp_f32_e32 v5, v5
	v_mul_f32_e32 v6, v197, v6
	v_sqrt_f32_e32 v6, v6
	v_exp_f32_e32 v8, v8
	v_mul_f32_e32 v7, v7, v164
	v_mul_f32_e32 v5, v5, v185
	v_exp_f32_e32 v24, v7
	v_add_f32_e32 v25, v25, v160
	v_mul_f32_e32 v185, v5, v6
	v_add_f32_e32 v5, 1.0, v8
	ds_read2st64_b32 v[6:7], v156 offset0:84 offset1:86
	v_mul_f32_e32 v25, 0xbfb8aa3b, v25
	v_rcp_f32_e32 v5, v5
	v_exp_f32_e32 v25, v25
	v_sub_f32_e32 v198, 1.0, v24
	v_add_f32_e32 v8, 1.0, v24
	v_mul_f32_e32 v8, v198, v8
	v_add_f32_e32 v9, v9, v130
	v_sqrt_f32_e32 v8, v8
	s_waitcnt lgkmcnt(0)
	v_mul_f32_e32 v5, v5, v6
	v_add_f32_e32 v6, 1.0, v25
	v_mul_f32_e32 v9, 0xbfb8aa3b, v9
	v_rcp_f32_e32 v6, v6
	v_exp_f32_e32 v9, v9
	v_mul_f32_e32 v199, v5, v8
	v_add_f32_e32 v8, v26, v160
	v_mul_f32_e32 v6, v6, v164
	v_add_f32_e32 v5, 1.0, v9
	v_mul_f32_e32 v8, 0xbfb8aa3b, v8
	v_exp_f32_e32 v25, v6
	v_rcp_f32_e32 v5, v5
	v_exp_f32_e32 v8, v8
	v_add_f32_e32 v9, v27, v160
	v_sub_f32_e32 v200, 1.0, v25
	v_add_f32_e32 v6, 1.0, v25
	v_mul_f32_e32 v5, v5, v7
	v_add_f32_e32 v7, 1.0, v8
	v_add_f32_e32 v8, v10, v130
	v_mul_f32_e32 v6, v200, v6
	v_rcp_f32_e32 v7, v7
	v_mul_f32_e32 v8, 0xbfb8aa3b, v8
	v_sqrt_f32_e32 v6, v6
	v_exp_f32_e32 v8, v8
	v_mul_f32_e32 v7, v7, v164
	v_exp_f32_e32 v26, v7
	v_mul_f32_e32 v201, v5, v6
	v_add_f32_e32 v5, 1.0, v8
	ds_read2st64_b32 v[6:7], v156 offset0:96 offset1:98
	v_mul_f32_e32 v9, 0xbfb8aa3b, v9
	v_rcp_f32_e32 v5, v5
	v_exp_f32_e32 v9, v9
	v_sub_f32_e32 v202, 1.0, v26
	v_add_f32_e32 v8, 1.0, v26
	s_waitcnt lgkmcnt(0)
	v_mul_f32_e32 v203, v5, v6
	v_add_f32_e32 v5, 1.0, v9
	v_add_f32_e32 v6, v11, v130
	v_rcp_f32_e32 v5, v5
	v_mul_f32_e32 v6, 0xbfb8aa3b, v6
	v_exp_f32_e32 v6, v6
	v_mul_f32_e32 v8, v202, v8
	v_sqrt_f32_e32 v27, v8
	v_mul_f32_e32 v5, v5, v164
	v_add_f32_e32 v8, v28, v160
	v_exp_f32_e32 v204, v5
	v_add_f32_e32 v5, 1.0, v6
	v_mul_f32_e32 v8, 0xbfb8aa3b, v8
	v_rcp_f32_e32 v5, v5
	v_exp_f32_e32 v8, v8
	v_sub_f32_e32 v206, 1.0, v204
	v_add_f32_e32 v6, 1.0, v204
	v_mul_f32_e32 v5, v5, v7
	v_add_f32_e32 v7, 1.0, v8
	v_add_f32_e32 v8, v12, v130
	v_mul_f32_e32 v6, v206, v6
	v_rcp_f32_e32 v7, v7
	v_mul_f32_e32 v8, 0xbfb8aa3b, v8
	v_sqrt_f32_e32 v6, v6
	v_exp_f32_e32 v8, v8
	v_mul_f32_e32 v7, v7, v164
	v_add_f32_e32 v9, v29, v160
	v_exp_f32_e32 v28, v7
	v_mul_f32_e32 v207, v5, v6
	v_add_f32_e32 v5, 1.0, v8
	ds_read2st64_b32 v[6:7], v156 offset0:100 offset1:102
	v_mul_f32_e32 v9, 0xbfb8aa3b, v9
	v_rcp_f32_e32 v5, v5
	v_exp_f32_e32 v9, v9
	v_sub_f32_e32 v12, 1.0, v28
	v_add_f32_e32 v8, 1.0, v28
	v_mul_f32_e32 v8, v12, v8
	s_waitcnt lgkmcnt(0)
	v_mul_f32_e32 v5, v5, v6
	v_add_f32_e32 v6, 1.0, v9
	v_add_f32_e32 v9, v13, v130
	v_sqrt_f32_e32 v8, v8
	v_mul_f32_e32 v9, 0xbfb8aa3b, v9
	v_rcp_f32_e32 v6, v6
	v_exp_f32_e32 v9, v9
	v_mul_f32_e32 v208, v5, v8
	v_add_f32_e32 v8, v30, v160
	v_mul_f32_e32 v6, v6, v164
	v_add_f32_e32 v5, 1.0, v9
	v_mul_f32_e32 v8, 0xbfb8aa3b, v8
	v_exp_f32_e32 v29, v6
	v_rcp_f32_e32 v5, v5
	v_exp_f32_e32 v8, v8
	v_add_f32_e32 v9, v31, v160
	v_sub_f32_e32 v13, 1.0, v29
	v_add_f32_e32 v6, 1.0, v29
	v_mul_f32_e32 v5, v5, v7
	v_add_f32_e32 v7, 1.0, v8
	v_add_f32_e32 v8, v14, v130
	v_mul_f32_e32 v6, v13, v6
	v_rcp_f32_e32 v7, v7
	v_mul_f32_e32 v8, 0xbfb8aa3b, v8
	v_sqrt_f32_e32 v6, v6
	v_exp_f32_e32 v8, v8
	v_mul_f32_e32 v7, v7, v164
	v_exp_f32_e32 v30, v7
	v_mul_f32_e32 v209, v5, v6
	v_add_f32_e32 v5, 1.0, v8
	ds_read2st64_b32 v[6:7], v156 offset0:112 offset1:114
	v_mul_f32_e32 v9, 0xbfb8aa3b, v9
	v_rcp_f32_e32 v5, v5
	v_exp_f32_e32 v9, v9
	v_sub_f32_e32 v14, 1.0, v30
	v_add_f32_e32 v8, 1.0, v30
	s_waitcnt lgkmcnt(0)
; DI unsigned pk_bf16(float lo, float hi) { f32x2 v = {lo, hi}; hbf16x2 r = __builtin_convertvector(v, hbf16x2); return __builtin_bit_cast(unsigned, r); }
; #define LRU_STEP(A_, B_, a_, b_) do { const float nf_ = fmaf((a_), (B_), (b_)), nb_ = fmaf((A_), (b_), (B_)); (B_) = d ? nb_ : nf_; (A_) *= (a_); } while (0)
; template <int PASS>
; DI void lru_units(const Params& p, LAS unsigned char* lds, int G, int bid) {
;     ...
;                 for (int i = 0; i < 16; ++i) {
;                     const int t = 32 * mt + (i & 3) + 8 * (i >> 2) + 4 * h;
;                     const float r = __builtin_amdgcn_rcpf(1.0f + __builtin_amdgcn_exp2f(-LOG2E * (acc[0][mt][i] + ga_b)));
;                     const float ig = __builtin_amdgcn_rcpf(1.0f + __builtin_amdgcn_exp2f(-LOG2E * (acc[1][mt][i] + gx_b)));
;                     const float a = __builtin_amdgcn_exp2f(-sp8l2 * r);
;                     const float bb = __builtin_amdgcn_sqrtf((1.0f - a) * (1.0f + a)) * (ig * U32[t * 128 + ch]);
;                     acc[0][mt][i] = a; acc[1][mt][i] = bb;
;                 }
;         }
;         if (PASS == 1) {
; #pragma unroll
;             for (int mt = 0; mt < 2; ++mt)
; #pragma unroll
;                 for (int i = 0; i < 16; ++i) { const int t = 32 * mt + (i & 3) + 8 * (i >> 2) + 4 * h;
;                     ABG[((((size_t)(b * NCHUNK + ci) * 8 + n) * 2 + d) * 64 + t) * 128 + ch] = pk_bf16(1.0f - acc[0][mt][i], acc[1][mt][i]); }
;     ...
;             float GA[8], GB[8];
; #pragma unroll
;             for (int k = 0; k < 8; ++k) {
;                 const int mt = k >> 2, g = k & 3; float A = 1.f, B = 0.f;
; #pragma unroll
;                 for (int e = 0; e < 4; ++e) LRU_STEP(A, B, acc[0][mt][4 * g + e], acc[1][mt][4 * g + e]);
;                 GA[k] = A; GB[k] = B;
	v_mul_f32_e32 v210, v5, v6
	v_add_f32_e32 v5, 1.0, v9
	v_rcp_f32_e32 v5, v5
	v_add_f32_e32 v6, v15, v130
	v_mul_f32_e32 v6, 0xbfb8aa3b, v6
	v_exp_f32_e32 v6, v6
	v_mul_f32_e32 v5, v5, v164
	v_exp_f32_e32 v211, v5
	v_mul_f32_e32 v8, v14, v8
	v_sqrt_f32_e32 v31, v8
	v_add_f32_e32 v8, v32, v160
	v_add_f32_e32 v5, 1.0, v6
	v_mul_f32_e32 v8, 0xbfb8aa3b, v8
	v_rcp_f32_e32 v5, v5
	v_sub_f32_e32 v15, 1.0, v211
	v_add_f32_e32 v6, 1.0, v211
	v_exp_f32_e32 v8, v8
	v_mul_f32_e32 v6, v15, v6
	v_sqrt_f32_e32 v6, v6
	v_mul_f32_e32 v5, v5, v7
	v_add_f32_e32 v7, 1.0, v8
	v_rcp_f32_e32 v7, v7
	v_mul_f32_e32 v213, v5, v6
	v_add_f32_e32 v6, v33, v160
	v_mul_f32_e32 v6, 0xbfb8aa3b, v6
	v_exp_f32_e32 v6, v6
	v_mul_f32_e32 v7, v7, v164
	v_add_f32_e32 v8, v16, v130
	v_exp_f32_e32 v32, v7
	v_mul_f32_e32 v8, 0xbfb8aa3b, v8
	v_exp_f32_e32 v8, v8
	v_add_f32_e32 v6, 1.0, v6
	v_rcp_f32_e32 v6, v6
	v_sub_f32_e32 v214, 1.0, v32
	v_add_f32_e32 v7, 1.0, v32
	v_mul_f32_e32 v7, v214, v7
	v_add_f32_e32 v5, 1.0, v8
	v_sqrt_f32_e32 v8, v7
	v_add_f32_e32 v7, v17, v130
	v_exp_f32_e32 v34, v34
	v_mul_f32_e32 v7, 0xbfb8aa3b, v7
	v_mul_f32_e32 v6, v6, v164
	v_exp_f32_e32 v9, v7
	v_exp_f32_e32 v33, v6
	v_sub_f32_e32 v162, 1.0, v34
	v_add_f32_e32 v50, 1.0, v34
	ds_read2st64_b32 v[6:7], v156 offset0:116 offset1:118
	v_mul_f32_e32 v50, v162, v50
	v_rcp_f32_e32 v5, v5
	v_add_f32_e32 v9, 1.0, v9
	v_sub_f32_e32 v160, 1.0, v33
	v_add_f32_e32 v10, 1.0, v33
	v_sqrt_f32_e32 v50, v50
	v_rcp_f32_e32 v9, v9
	v_mul_f32_e32 v10, v160, v10
	v_sqrt_f32_e32 v10, v10
	s_waitcnt lgkmcnt(0)
	v_mul_f32_e32 v5, v5, v6
	v_mul_f32_e32 v139, v51, v50
	v_sqrt_f32_e32 v55, v55
	v_mul_f32_e32 v215, v5, v8
	v_mul_f32_e32 v5, v9, v7
	v_lshl_add_u64 v[6:7], v[136:137], 0, s[0:1]
	v_lshl_or_b32 v130, s91, 16, v157
	v_mul_f32_e32 v216, v5, v10
	v_cvt_pk_bf16_f32 v5, v162, v139
	v_lshl_add_u64 v[6:7], v[6:7], 0, v[130:131]
	global_store_dword v[6:7], v5, off
	v_cvt_pk_bf16_f32 v5, v165, v52
	v_add_co_u32_e32 v8, vcc, s31, v6
	global_store_dword v[6:7], v5, off offset:512
	v_cvt_pk_bf16_f32 v5, v166, v53
	v_addc_co_u32_e32 v9, vcc, 0, v7, vcc
	v_mul_f32_e32 v163, v161, v55
	v_sqrt_f32_e32 v59, v59
	global_store_dword v[6:7], v5, off offset:1024
	v_cvt_pk_bf16_f32 v5, v167, v54
	v_add_co_u32_e32 v10, vcc, s34, v6
	global_store_dword v[6:7], v5, off offset:1536
	v_cvt_pk_bf16_f32 v5, v170, v163
	v_addc_co_u32_e32 v11, vcc, 0, v7, vcc
	global_store_dword v[10:11], v5, off offset:-4096
	v_cvt_pk_bf16_f32 v5, v171, v56
	global_store_dword v[8:9], v5, off offset:512
	v_cvt_pk_bf16_f32 v5, v172, v57
	v_mul_f32_e32 v169, v168, v59
	global_store_dword v[8:9], v5, off offset:1024
	v_cvt_pk_bf16_f32 v5, v173, v58
	v_sqrt_f32_e32 v63, v63
	global_store_dword v[8:9], v5, off offset:1536
	v_cvt_pk_bf16_f32 v5, v176, v169
	global_store_dword v[10:11], v5, off
	v_cvt_pk_bf16_f32 v5, v177, v60
	global_store_dword v[10:11], v5, off offset:512
	v_cvt_pk_bf16_f32 v5, v178, v61
	v_add_co_u32_e32 v8, vcc, s35, v6
	global_store_dword v[10:11], v5, off offset:1024
	v_cvt_pk_bf16_f32 v5, v180, v62
	v_addc_co_u32_e32 v9, vcc, 0, v7, vcc
	v_mul_f32_e32 v175, v174, v63
	v_sqrt_f32_e32 v19, v19
	global_store_dword v[10:11], v5, off offset:1536
	v_add_co_u32_e32 v10, vcc, s67, v6
	v_cvt_pk_bf16_f32 v5, v182, v175
	s_nop 0
	v_addc_co_u32_e32 v11, vcc, 0, v7, vcc
	global_store_dword v[10:11], v5, off offset:-4096
	v_cvt_pk_bf16_f32 v5, v183, v64
	global_store_dword v[8:9], v5, off offset:512
	v_cvt_pk_bf16_f32 v5, v186, v65
	v_mul_f32_e32 v181, v179, v19
	global_store_dword v[8:9], v5, off offset:1024
	v_cvt_pk_bf16_f32 v5, v187, v18
	global_store_dword v[8:9], v5, off offset:1536
	v_cvt_pk_bf16_f32 v5, v188, v181
	global_store_dword v[10:11], v5, off
	v_cvt_pk_bf16_f32 v5, v189, v20
	global_store_dword v[10:11], v5, off offset:512
	v_cvt_pk_bf16_f32 v5, v191, v190
	v_add_co_u32_e32 v8, vcc, s88, v6
	global_store_dword v[10:11], v5, off offset:1024
	v_cvt_pk_bf16_f32 v5, v192, v193
	v_addc_co_u32_e32 v9, vcc, 0, v7, vcc
	v_mul_f32_e32 v196, v184, v195
	global_store_dword v[10:11], v5, off offset:1536
	v_add_co_u32_e32 v10, vcc, s89, v6
	v_cvt_pk_bf16_f32 v5, v194, v196
	s_nop 0
	v_addc_co_u32_e32 v11, vcc, 0, v7, vcc
	global_store_dword v[10:11], v5, off offset:-4096
	v_cvt_pk_bf16_f32 v5, v197, v185
	global_store_dword v[8:9], v5, off offset:512
	v_cvt_pk_bf16_f32 v5, v198, v199
	v_mul_f32_e32 v205, v203, v27
	global_store_dword v[8:9], v5, off offset:1024
	v_cvt_pk_bf16_f32 v5, v200, v201
	global_store_dword v[8:9], v5, off offset:1536
	v_cvt_pk_bf16_f32 v5, v202, v205
	v_fmac_f32_e32 v163, 0, v38
	v_fma_f32 v8, v161, v55, 0
	global_store_dword v[10:11], v5, off
	v_cvt_pk_bf16_f32 v5, v206, v207
	v_cndmask_b32_e64 v8, v8, v163, s[2:3]
	global_store_dword v[10:11], v5, off offset:512
	v_cvt_pk_bf16_f32 v5, v12, v208
	v_fma_f32 v9, v39, v8, v56
	v_fmac_f32_e32 v8, v38, v56
	global_store_dword v[10:11], v5, off offset:1024
	v_cvt_pk_bf16_f32 v5, v13, v209
	v_cndmask_b32_e64 v8, v8, v9, s[2:3]
	v_mul_f32_e32 v9, v38, v39
	global_store_dword v[10:11], v5, off offset:1536
	v_fma_f32 v10, v40, v8, v57
	v_fmac_f32_e32 v8, v9, v57
	v_cndmask_b32_e64 v8, v8, v10, s[2:3]
	v_mul_f32_e32 v9, v40, v9
	v_fma_f32 v10, v41, v8, v58
	v_fmac_f32_e32 v8, v9, v58
	v_cndmask_b32_e64 v8, v8, v10, s[2:3]
	v_fmac_f32_e32 v169, 0, v42
	v_fma_f32 v10, v168, v59, 0
	v_cndmask_b32_e64 v10, v10, v169, s[2:3]
	v_fma_f32 v11, v43, v10, v60
	v_fmac_f32_e32 v10, v42, v60
	v_cndmask_b32_e64 v10, v10, v11, s[2:3]
	v_mul_f32_e32 v11, v42, v43
	v_fma_f32 v12, v44, v10, v61
	v_fmac_f32_e32 v10, v11, v61
	v_cndmask_b32_e64 v10, v10, v12, s[2:3]
	v_mul_f32_e32 v11, v44, v11
; #define LRU_STEP(A_, B_, a_, b_) do { const float nf_ = fmaf((a_), (B_), (b_)), nb_ = fmaf((A_), (b_), (B_)); (B_) = d ? nb_ : nf_; (A_) *= (a_); } while (0)
; template <int PASS>
; DI void lru_units(const Params& p, LAS unsigned char* lds, int G, int bid) {
;     ...
;             float GA[8], GB[8];
; #pragma unroll
;             for (int k = 0; k < 8; ++k) {
;                 const int mt = k >> 2, g = k & 3; float A = 1.f, B = 0.f;
; #pragma unroll
;                 for (int e = 0; e < 4; ++e) LRU_STEP(A, B, acc[0][mt][4 * g + e], acc[1][mt][4 * g + e]);
;                 GA[k] = A; GB[k] = B;
;             }
;             float TA = 1.f, TB = 0.f;
; #pragma unroll
;             for (int k = 0; k < 8; ++k) {
;                 const float pa = __shfl_xor(GA[k], 32), pb = __shfl_xor(GB[k], 32);
;                 const float la = h ? pa : GA[k], lb = h ? pb : GB[k], ha = h ? GA[k] : pa, hb = h ? GB[k] : pb;
;                 LRU_STEP(TA, TB, la, lb); LRU_STEP(TA, TB, ha, hb);
;             }
;     ...
;             if (h == 0) SUMM[((size_t)(d * NB + b) * NCHUNK + ci) * 1024 + chg] = (f32x2){TA, TB};
	v_fma_f32 v12, v45, v10, v62
	v_fmac_f32_e32 v10, v11, v62
	v_cndmask_b32_e64 v10, v10, v12, s[2:3]
	v_fmac_f32_e32 v175, 0, v46
	v_fma_f32 v12, v174, v63, 0
	v_cndmask_b32_e64 v12, v12, v175, s[2:3]
	v_fma_f32 v13, v47, v12, v64
	v_fmac_f32_e32 v12, v46, v64
	v_mul_f32_e32 v212, v210, v31
	v_cndmask_b32_e64 v12, v12, v13, s[2:3]
	v_mul_f32_e32 v13, v46, v47
	v_cvt_pk_bf16_f32 v5, v14, v212
	v_fma_f32 v14, v48, v12, v65
	v_fmac_f32_e32 v12, v13, v65
	v_cndmask_b32_e64 v12, v12, v14, s[2:3]
	v_mul_f32_e32 v13, v48, v13
	v_fma_f32 v14, v49, v12, v18
	v_fmac_f32_e32 v12, v13, v18
	v_add_co_u32_e32 v164, vcc, s90, v6
	v_cndmask_b32_e64 v12, v12, v14, s[2:3]
	v_fmac_f32_e32 v181, 0, v2
	v_fma_f32 v14, v179, v19, 0
	v_addc_co_u32_e32 v165, vcc, 0, v7, vcc
	v_cndmask_b32_e64 v14, v14, v181, s[2:3]
	global_store_dword v[164:165], v5, off
	v_cvt_pk_bf16_f32 v5, v15, v213
	v_fma_f32 v15, v3, v14, v20
	v_fmac_f32_e32 v14, v2, v20
	v_cndmask_b32_e64 v14, v14, v15, s[2:3]
	v_mul_f32_e32 v2, v2, v3
	v_fma_f32 v3, v4, v14, v190
	v_fmac_f32_e32 v14, v2, v190
	v_cndmask_b32_e64 v3, v14, v3, s[2:3]
	v_mul_f32_e32 v4, v4, v2
	v_fma_f32 v2, v21, v3, v193
	v_fmac_f32_e32 v3, v4, v193
	v_cndmask_b32_e64 v2, v3, v2, s[2:3]
	v_mul_f32_e32 v3, v21, v4
	v_fmac_f32_e32 v196, 0, v22
	v_fma_f32 v4, v184, v195, 0
	v_cndmask_b32_e64 v4, v4, v196, s[2:3]
	v_fma_f32 v14, v23, v4, v185
	v_fmac_f32_e32 v4, v22, v185
	v_cndmask_b32_e64 v4, v4, v14, s[2:3]
	v_mul_f32_e32 v14, v22, v23
	v_fma_f32 v15, v24, v4, v199
	v_fmac_f32_e32 v4, v14, v199
	v_cndmask_b32_e64 v4, v4, v15, s[2:3]
	v_mul_f32_e32 v14, v24, v14
	v_fma_f32 v15, v25, v4, v201
	v_fmac_f32_e32 v4, v14, v201
	v_cndmask_b32_e64 v4, v4, v15, s[2:3]
	v_fmac_f32_e32 v205, 0, v26
	v_fma_f32 v15, v203, v27, 0
	v_cndmask_b32_e64 v15, v15, v205, s[2:3]
	v_fma_f32 v16, v204, v15, v207
	v_fmac_f32_e32 v15, v26, v207
	v_cndmask_b32_e64 v15, v15, v16, s[2:3]
	v_mul_f32_e32 v16, v26, v204
	v_fma_f32 v17, v28, v15, v208
	v_fmac_f32_e32 v15, v16, v208
	v_cndmask_b32_e64 v15, v15, v17, s[2:3]
	v_mul_f32_e32 v16, v28, v16
	v_fma_f32 v17, v29, v15, v209
	v_fmac_f32_e32 v15, v16, v209
	global_store_dword v[164:165], v5, off offset:512
	v_fmac_f32_e32 v139, 0, v34
	v_fma_f32 v5, v51, v50, 0
	v_cndmask_b32_e64 v15, v15, v17, s[2:3]
	v_fmac_f32_e32 v212, 0, v30
	v_fma_f32 v17, v210, v31, 0
	v_cndmask_b32_e64 v5, v5, v139, s[2:3]
	v_cndmask_b32_e64 v17, v17, v212, s[2:3]
	v_fma_f32 v6, v35, v5, v52
	v_fmac_f32_e32 v5, v34, v52
	v_fma_f32 v18, v211, v17, v213
	v_fmac_f32_e32 v17, v30, v213
	v_cndmask_b32_e64 v5, v5, v6, s[2:3]
	v_mul_f32_e32 v6, v34, v35
	v_cndmask_b32_e64 v17, v17, v18, s[2:3]
	v_mul_f32_e32 v18, v30, v211
	v_fma_f32 v7, v36, v5, v53
	v_fmac_f32_e32 v5, v6, v53
	v_fma_f32 v19, v32, v17, v215
	v_fmac_f32_e32 v17, v18, v215
	v_cndmask_b32_e64 v5, v5, v7, s[2:3]
	v_mul_f32_e32 v6, v36, v6
	v_cndmask_b32_e64 v17, v17, v19, s[2:3]
	v_mul_f32_e32 v18, v32, v18
	v_fma_f32 v7, v37, v5, v54
	v_fmac_f32_e32 v5, v6, v54
	v_fma_f32 v19, v33, v17, v216
	v_fmac_f32_e32 v17, v18, v216
	v_cndmask_b32_e64 v7, v5, v7, s[2:3]
	v_mul_f32_e32 v6, v37, v6
	v_mul_f32_e32 v9, v41, v9
	v_mul_f32_e32 v11, v45, v11
	v_mul_f32_e32 v13, v49, v13
	v_mul_f32_e32 v14, v25, v14
	v_mul_f32_e32 v16, v29, v16
	v_cndmask_b32_e64 v17, v17, v19, s[2:3]
	v_mul_f32_e32 v18, v33, v18
	ds_bpermute_b32 v34, v148, v6
	ds_bpermute_b32 v33, v148, v7
	ds_bpermute_b32 v32, v148, v9
	ds_bpermute_b32 v31, v148, v8
	ds_bpermute_b32 v30, v148, v11
	ds_bpermute_b32 v29, v148, v10
	ds_bpermute_b32 v28, v148, v13
	ds_bpermute_b32 v27, v148, v12
	ds_bpermute_b32 v26, v148, v3
	ds_bpermute_b32 v25, v148, v2
	ds_bpermute_b32 v24, v148, v14
	ds_bpermute_b32 v23, v148, v4
	ds_bpermute_b32 v22, v148, v16
	ds_bpermute_b32 v21, v148, v15
	ds_bpermute_b32 v20, v148, v18
	ds_bpermute_b32 v19, v148, v17
	v_cvt_pk_bf16_f32 v35, v214, v215
	global_store_dword v[164:165], v35, off offset:1024
	v_cvt_pk_bf16_f32 v35, v160, v216
	global_store_dword v[164:165], v35, off offset:1536
	s_and_saveexec_b64 s[0:1], s[4:5]
	s_cbranch_execz .LBB0_340
	v_fmac_f32_e32 v7, 0, v6
	v_add_f32_e32 v5, 0, v5
	v_cndmask_b32_e64 v5, v5, v7, s[2:3]
	s_waitcnt lgkmcnt(14)
	v_fma_f32 v7, v34, v5, v33
	v_fmac_f32_e32 v5, v6, v33
	v_mul_f32_e32 v35, v6, v34
	v_cndmask_b32_e64 v5, v5, v7, s[2:3]
	v_fma_f32 v6, v9, v5, v8
	v_fmac_f32_e32 v5, v35, v8
	v_mul_f32_e32 v37, v9, v35
	v_cndmask_b32_e64 v5, v5, v6, s[2:3]
	s_waitcnt lgkmcnt(12)
	v_fma_f32 v6, v32, v5, v31
	v_fmac_f32_e32 v5, v37, v31
	v_mul_f32_e32 v38, v37, v32
	v_cndmask_b32_e64 v5, v5, v6, s[2:3]
	v_fma_f32 v6, v11, v5, v10
	v_fmac_f32_e32 v5, v38, v10
	v_mul_f32_e32 v39, v11, v38
	v_cndmask_b32_e64 v5, v5, v6, s[2:3]
	s_waitcnt lgkmcnt(10)
	v_fma_f32 v6, v30, v5, v29
	v_fmac_f32_e32 v5, v39, v29
	v_mul_f32_e32 v40, v39, v30
	v_cndmask_b32_e64 v5, v5, v6, s[2:3]
	v_fma_f32 v6, v13, v5, v12
	v_fmac_f32_e32 v5, v40, v12
	v_mul_f32_e32 v41, v13, v40
	v_cndmask_b32_e64 v5, v5, v6, s[2:3]
	s_waitcnt lgkmcnt(8)
	v_fma_f32 v6, v28, v5, v27
	v_fmac_f32_e32 v5, v41, v27
	v_mul_f32_e32 v42, v41, v28
	v_cndmask_b32_e64 v5, v5, v6, s[2:3]
	v_mul_f32_e32 v43, v3, v42
	v_fma_f32 v3, v3, v5, v2
	v_fmac_f32_e32 v5, v42, v2
	v_cndmask_b32_e64 v2, v5, v3, s[2:3]
	s_waitcnt lgkmcnt(6)
	v_fma_f32 v3, v26, v2, v25
	v_fmac_f32_e32 v2, v43, v25
	v_mul_f32_e32 v44, v43, v26
	v_cndmask_b32_e64 v2, v2, v3, s[2:3]
	v_fma_f32 v3, v14, v2, v4
	v_fmac_f32_e32 v2, v44, v4
	v_mul_f32_e32 v45, v14, v44
	v_cndmask_b32_e64 v2, v2, v3, s[2:3]
	s_waitcnt lgkmcnt(4)
	v_fma_f32 v3, v24, v2, v23
	v_fmac_f32_e32 v2, v45, v23
	v_mul_f32_e32 v46, v45, v24
	v_cndmask_b32_e64 v2, v2, v3, s[2:3]
	v_fma_f32 v3, v16, v2, v15
	v_fmac_f32_e32 v2, v46, v15
	v_mul_f32_e32 v47, v16, v46
	v_cndmask_b32_e64 v2, v2, v3, s[2:3]
	s_waitcnt lgkmcnt(2)
	v_fma_f32 v3, v22, v2, v21
	v_fmac_f32_e32 v2, v47, v21
	v_mul_f32_e32 v48, v47, v22
	v_cndmask_b32_e64 v2, v2, v3, s[2:3]
	v_fma_f32 v3, v18, v2, v17
	v_fmac_f32_e32 v2, v48, v17
	v_mul_f32_e32 v49, v18, v48
	v_cndmask_b32_e64 v2, v2, v3, s[2:3]
	s_waitcnt lgkmcnt(0)
	v_fma_f32 v3, v20, v2, v19
	v_fmac_f32_e32 v2, v49, v19
	v_cndmask_b32_e64 v37, v2, v3, s[2:3]
	v_or_b32_e32 v2, s13, v146
	v_mul_u32_u24_e32 v130, 36, v2
	s_ashr_i32 s13, s12, 31
	v_lshl_add_u64 v[2:3], v[130:131], 0, s[12:13]
	v_lshlrev_b64 v[2:3], 13, v[2:3]
	v_lshl_add_u64 v[2:3], s[10:11], 0, v[2:3]
	v_lshlrev_b32_e32 v130, 3, v159
	v_mul_f32_e32 v36, v49, v20
	v_lshl_add_u64 v[2:3], v[2:3], 0, v[130:131]
	global_store_dwordx2 v[2:3], v[36:37], off
	s_branch .LBB0_340
